# out-proj GEMM: first K double-step peeled with C=0, accumulator zeroing at the tile top removed
# baseline (speedup 1.0000x reference)
; #define PG8_SETA(d0, d1, u) do { d0.x = PG8_OFFA(u, Rr[0], 0); d0.y = PG8_OFFA(u, Rr[1], 1); d1.x = PG8_OFFA(u, HALF + Rr[0], 0); d1.y = PG8_OFFA(u, HALF + Rr[1], 1); } while (0)
; #define PG8_STAGE_A(bufoff, soff, voff) do { _Pragma("unroll") for (int _i = 0; _i < 2; ++_i) \
;         __builtin_amdgcn_raw_ptr_buffer_load_lds(rsA, (LAS void*)(lds + (bufoff) + ldsw + _i * 8192), 16, (voff)[_i], (soff), 0, 0); } while (0)
; #define PG8_STAGE_B(bufoff, soff) do { _Pragma("unroll") for (int _i = 0; _i < 2; ++_i) \
;         __builtin_amdgcn_raw_ptr_buffer_load_lds(rsB, (LAS void*)(lds + (bufoff) + ldsw + _i * 8192), 16, voffB[_i], (soff), 0, 0); } while (0)
; #define PG8_LDA(dst, b, h) do { _Pragma("unroll") for (int m = 0; m < 4; ++m) dst[m] = PG8_LD8(lds + PG8_SA(b, h) + aoff + m * 2048); } while (0)
; #define PG8_LDB(dst, b, h) do { _Pragma("unroll") for (int n = 0; n < 2; ++n) dst[n] = PG8_LD8(lds + PG8_SB(b, h) + boff + n * 2048); } while (0)
; #define PG8_WAIT_V(n) asm volatile("s_waitcnt vmcnt(" #n ")" ::: "memory")
; template <class Epi, class Sched, bool GATHER, bool ALIGN_EPI, bool SP2, bool FP8>
; __device__ __forceinline__ void gemm_phase(LAS unsigned char* lds, const Gemm g, const Sched& S, const Epi& E) {
;     ...
;         const bool has_next = S.next(ui + 1, nxt);
;         const int nA = has_next ? (GATHER ? 0 : nxt.pm * tstep) : cA, nB = has_next ? nxt.pn * tstep : cB;
;         u32x2 nvA0 = vA0, nvA1 = vA1;
;         if constexpr (GATHER) { if (has_next) PG8_SETA(nvA0, nvA1, nxt); }
;         for (int t = 0; t < nt; t += 2) {
;             const bool last = (t == nt - 2);
;             if (last) pre = E.prefetch(cur, wr, wc, fr, fq);
;             const int a1 = cA + (t + 1) * kstep;
;             const int a2 = last ? nA : cA + (t + 2) * kstep, b2 = last ? nB : cB + (t + 2) * kstep;
;             const int a3 = a2 + kstep, b3 = b2 + kstep;
;             const u32x2 va20 = (GATHER && last) ? nvA0 : vA0, va21 = (GATHER && last) ? nvA1 : vA1;
;             if constexpr (SP2) {
;             PG8_LDB(B0, 0, 0); PG8_LDB(B1, 0, 1); PG8_SCHED; PG8_LDA(At, 0, 0); PG8_STAGE_A(PG8_SA(1, 1), a1, vA1);
;             PG8_WAIT_V(8); PG8_WAIT_L(0); PG8_BAR; PG8_MMA(0, 0, At, B0); PG8_MMA(0, 1, At, B1); PG8_BAR; PG8_SCHED;
;             PG8_LDA(At, 0, 1); PG8_STAGE_B(PG8_SB(0, 0), b2); PG8_STAGE_B(PG8_SB(0, 1), b2 + hstep); PG8_STAGE_A(PG8_SA(0, 0), a2, va20);
.LBB0_707:
	v_cmp_lt_i64_e32 vcc, s[10:11], v[164:165]
	s_lshl_b32 s70, s31, 20
	s_and_b64 s[10:11], vcc, exec
	s_cselect_b32 s75, s70, s77
	s_lshl_b32 s71, s30, 20
	s_and_b64 s[10:11], vcc, exec
	s_mov_b32 s55, s94
	s_cselect_b32 s76, s71, s78
	s_addk_i32 s77, 0x80
	s_addk_i32 s78, 0x100
	s_mov_b32 s79, -2
	ds_read_b128 v[158:161], v172
	ds_read_b128 v[154:157], v172 offset:1024
	ds_read_b128 v[150:153], v172 offset:2048
	ds_read_b128 v[146:149], v172 offset:3072
	ds_read_b128 v[142:145], v173
	ds_read_b128 v[138:141], v173 offset:1024
	ds_read_b128 v[134:137], v173 offset:2048
	ds_read_b128 v[130:133], v173 offset:3072
	s_add_i32 s10, s77, 0x80
	s_cmp_eq_u32 s79, 28
	s_cselect_b32 s82, s75, s10
	s_cselect_b32 s81, s76, s78
	s_or_b32 s80, s82, 0x80
	s_mov_b32 m0, s52
	ds_read_b128 v[178:181], v174
	ds_read_b128 v[182:185], v174 offset:1024
	ds_read_b128 v[186:189], v174 offset:2048
	ds_read_b128 v[190:193], v174 offset:3072
	ds_read_b128 v[194:197], v174 offset:4096
	ds_read_b128 v[198:201], v174 offset:5120
	ds_read_b128 v[202:205], v174 offset:6144
	ds_read_b128 v[206:209], v174 offset:7168
	buffer_load_dwordx4 v170, s[4:7], s77 offen lds
	s_mov_b32 m0, s53
	s_nop 0
	buffer_load_dwordx4 v171, s[4:7], s77 offen lds
	s_waitcnt vmcnt(8)
	s_waitcnt lgkmcnt(0)
	s_barrier
	s_setprio 1
	s_waitcnt lgkmcnt(0)
	v_mfma_f32_16x16x32_bf16 v[126:129], v[158:161], v[178:181], 0
	s_nop 0
	v_mfma_f32_16x16x32_bf16 v[126:129], v[154:157], v[182:185], v[126:129]
	v_mfma_f32_16x16x32_bf16 v[122:125], v[150:153], v[178:181], 0
	s_nop 0
	v_mfma_f32_16x16x32_bf16 v[122:125], v[146:149], v[182:185], v[122:125]
	v_mfma_f32_16x16x32_bf16 v[110:113], v[158:161], v[186:189], 0
	s_nop 0
	v_mfma_f32_16x16x32_bf16 v[110:113], v[154:157], v[190:193], v[110:113]
	v_mfma_f32_16x16x32_bf16 v[106:109], v[150:153], v[186:189], 0
	s_nop 0
	v_mfma_f32_16x16x32_bf16 v[106:109], v[146:149], v[190:193], v[106:109]
	v_mfma_f32_16x16x32_bf16 v[94:97], v[158:161], v[194:197], 0
	s_nop 0
	v_mfma_f32_16x16x32_bf16 v[94:97], v[154:157], v[198:201], v[94:97]
	v_mfma_f32_16x16x32_bf16 v[90:93], v[150:153], v[194:197], 0
	s_nop 0
	v_mfma_f32_16x16x32_bf16 v[90:93], v[146:149], v[198:201], v[90:93]
	v_mfma_f32_16x16x32_bf16 v[78:81], v[158:161], v[202:205], 0
	s_nop 0
	v_mfma_f32_16x16x32_bf16 v[78:81], v[154:157], v[206:209], v[78:81]
	v_mfma_f32_16x16x32_bf16 v[74:77], v[150:153], v[202:205], 0
	s_nop 0
	v_mfma_f32_16x16x32_bf16 v[74:77], v[146:149], v[206:209], v[74:77]
	s_setprio 0
	s_setprio 1
	v_mfma_f32_16x16x32_bf16 v[118:121], v[142:145], v[178:181], 0
	s_nop 0
	v_mfma_f32_16x16x32_bf16 v[118:121], v[138:141], v[182:185], v[118:121]
	v_mfma_f32_16x16x32_bf16 v[114:117], v[134:137], v[178:181], 0
	s_nop 0
	v_mfma_f32_16x16x32_bf16 v[114:117], v[130:133], v[182:185], v[114:117]
	v_mfma_f32_16x16x32_bf16 v[102:105], v[142:145], v[186:189], 0
	s_nop 0
	v_mfma_f32_16x16x32_bf16 v[102:105], v[138:141], v[190:193], v[102:105]
	v_mfma_f32_16x16x32_bf16 v[98:101], v[134:137], v[186:189], 0
	s_nop 0
	v_mfma_f32_16x16x32_bf16 v[98:101], v[130:133], v[190:193], v[98:101]
	v_mfma_f32_16x16x32_bf16 v[86:89], v[142:145], v[194:197], 0
	s_nop 0
	v_mfma_f32_16x16x32_bf16 v[86:89], v[138:141], v[198:201], v[86:89]
	v_mfma_f32_16x16x32_bf16 v[82:85], v[134:137], v[194:197], 0
	s_nop 0
	v_mfma_f32_16x16x32_bf16 v[82:85], v[130:133], v[198:201], v[82:85]
	v_mfma_f32_16x16x32_bf16 v[70:73], v[142:145], v[202:205], 0
	s_nop 0
	v_mfma_f32_16x16x32_bf16 v[70:73], v[138:141], v[206:209], v[70:73]
	v_mfma_f32_16x16x32_bf16 v[66:69], v[134:137], v[202:205], 0
	s_nop 0
	v_mfma_f32_16x16x32_bf16 v[66:69], v[130:133], v[206:209], v[66:69]
	s_setprio 0
	s_barrier
	s_mov_b32 m0, s37
	s_mov_b32 s10, s6
	s_mov_b32 s11, s7
	ds_read_b128 v[178:181], v174 offset:16384
	ds_read_b128 v[182:185], v174 offset:17408
	ds_read_b128 v[186:189], v174 offset:18432
	ds_read_b128 v[190:193], v174 offset:19456
	ds_read_b128 v[194:197], v174 offset:20480
	ds_read_b128 v[198:201], v174 offset:21504
	ds_read_b128 v[202:205], v174 offset:22528
	ds_read_b128 v[206:209], v174 offset:23552
	buffer_load_dwordx4 v1, s[8:11], s81 offen lds
	s_mov_b32 m0, s38
	s_add_i32 s83, s81, 0x80000
	buffer_load_dwordx4 v163, s[8:11], s81 offen lds
	s_mov_b32 m0, s39
	s_nop 0
	buffer_load_dwordx4 v1, s[8:11], s83 offen lds
	s_mov_b32 m0, s40
	s_nop 0
	buffer_load_dwordx4 v163, s[8:11], s83 offen lds
	s_mov_b32 m0, s36
	s_nop 0
	buffer_load_dwordx4 v168, s[4:7], s82 offen lds
	s_mov_b32 m0, s41
	s_nop 0
	buffer_load_dwordx4 v169, s[4:7], s82 offen lds
	s_waitcnt vmcnt(8)
	s_waitcnt lgkmcnt(0)
	s_barrier
; #define PG8_STAGE_A(bufoff, soff, voff) do { _Pragma("unroll") for (int _i = 0; _i < 2; ++_i) \
;         __builtin_amdgcn_raw_ptr_buffer_load_lds(rsA, (LAS void*)(lds + (bufoff) + ldsw + _i * 8192), 16, (voff)[_i], (soff), 0, 0); } while (0)
; #define PG8_LDA(dst, b, h) do { _Pragma("unroll") for (int m = 0; m < 4; ++m) dst[m] = PG8_LD8(lds + PG8_SA(b, h) + aoff + m * 2048); } while (0)
; #define PG8_LDB(dst, b, h) do { _Pragma("unroll") for (int n = 0; n < 2; ++n) dst[n] = PG8_LD8(lds + PG8_SB(b, h) + boff + n * 2048); } while (0)
; #define PG8_WAIT_V(n) asm volatile("s_waitcnt vmcnt(" #n ")" ::: "memory")
; #define PG8_WAIT_L(n) asm volatile("s_waitcnt lgkmcnt(" #n ")" ::: "memory")
; #define PG8_BAR __builtin_amdgcn_s_barrier()
; #define PG8_SCHED __builtin_amdgcn_sched_barrier(0)
; template <class Epi, class Sched, bool GATHER, bool ALIGN_EPI, bool SP2, bool FP8>
; __device__ __forceinline__ void gemm_phase(LAS unsigned char* lds, const Gemm g, const Sched& S, const Epi& E) {
;     ...
;             PG8_WAIT_V(8); PG8_WAIT_L(0); PG8_BAR; PG8_MMA(1, 0, At, B0); PG8_MMA(1, 1, At, B1); PG8_BAR; PG8_SCHED;
;             PG8_LDB(B0, 1, 0); PG8_LDB(B1, 1, 1); PG8_SCHED; PG8_LDA(At, 1, 0); PG8_STAGE_A(PG8_SA(0, 1), a2, va21);
;             PG8_WAIT_V(8); PG8_WAIT_L(0); PG8_BAR; PG8_MMA(0, 0, At, B0); PG8_MMA(0, 1, At, B1); PG8_BAR; PG8_SCHED;
	s_setprio 1
	s_waitcnt lgkmcnt(7)
	v_mfma_f32_16x16x32_bf16 v[62:65], v[158:161], v[178:181], 0
	s_waitcnt lgkmcnt(6)
	v_mfma_f32_16x16x32_bf16 v[62:65], v[154:157], v[182:185], v[62:65]
	v_mfma_f32_16x16x32_bf16 v[58:61], v[150:153], v[178:181], 0
	s_nop 0
	v_mfma_f32_16x16x32_bf16 v[58:61], v[146:149], v[182:185], v[58:61]
	s_waitcnt lgkmcnt(5)
	v_mfma_f32_16x16x32_bf16 v[46:49], v[158:161], v[186:189], 0
	s_waitcnt lgkmcnt(4)
	v_mfma_f32_16x16x32_bf16 v[46:49], v[154:157], v[190:193], v[46:49]
	v_mfma_f32_16x16x32_bf16 v[42:45], v[150:153], v[186:189], 0
	s_nop 0
	v_mfma_f32_16x16x32_bf16 v[42:45], v[146:149], v[190:193], v[42:45]
	s_waitcnt lgkmcnt(3)
	v_mfma_f32_16x16x32_bf16 v[30:33], v[158:161], v[194:197], 0
	s_waitcnt lgkmcnt(2)
	v_mfma_f32_16x16x32_bf16 v[30:33], v[154:157], v[198:201], v[30:33]
	v_mfma_f32_16x16x32_bf16 v[26:29], v[150:153], v[194:197], 0
	s_nop 0
	v_mfma_f32_16x16x32_bf16 v[26:29], v[146:149], v[198:201], v[26:29]
	s_waitcnt lgkmcnt(1)
	v_mfma_f32_16x16x32_bf16 v[14:17], v[158:161], v[202:205], 0
	s_waitcnt lgkmcnt(0)
	v_mfma_f32_16x16x32_bf16 v[14:17], v[154:157], v[206:209], v[14:17]
	v_mfma_f32_16x16x32_bf16 v[10:13], v[150:153], v[202:205], 0
	s_nop 0
	v_mfma_f32_16x16x32_bf16 v[10:13], v[146:149], v[206:209], v[10:13]
	s_setprio 0
	s_setprio 1
	v_mfma_f32_16x16x32_bf16 v[54:57], v[142:145], v[178:181], 0
	s_nop 0
	v_mfma_f32_16x16x32_bf16 v[54:57], v[138:141], v[182:185], v[54:57]
	v_mfma_f32_16x16x32_bf16 v[50:53], v[134:137], v[178:181], 0
	s_nop 0
	v_mfma_f32_16x16x32_bf16 v[50:53], v[130:133], v[182:185], v[50:53]
	v_mfma_f32_16x16x32_bf16 v[38:41], v[142:145], v[186:189], 0
	s_nop 0
	v_mfma_f32_16x16x32_bf16 v[38:41], v[138:141], v[190:193], v[38:41]
	v_mfma_f32_16x16x32_bf16 v[34:37], v[134:137], v[186:189], 0
	s_nop 0
	v_mfma_f32_16x16x32_bf16 v[34:37], v[130:133], v[190:193], v[34:37]
	v_mfma_f32_16x16x32_bf16 v[22:25], v[142:145], v[194:197], 0
	s_nop 0
	v_mfma_f32_16x16x32_bf16 v[22:25], v[138:141], v[198:201], v[22:25]
	v_mfma_f32_16x16x32_bf16 v[18:21], v[134:137], v[194:197], 0
	s_nop 0
	v_mfma_f32_16x16x32_bf16 v[18:21], v[130:133], v[198:201], v[18:21]
	v_mfma_f32_16x16x32_bf16 v[6:9], v[142:145], v[202:205], 0
	s_nop 0
	v_mfma_f32_16x16x32_bf16 v[6:9], v[138:141], v[206:209], v[6:9]
	v_mfma_f32_16x16x32_bf16 v[2:5], v[134:137], v[202:205], 0
	s_nop 0
	v_mfma_f32_16x16x32_bf16 v[2:5], v[130:133], v[206:209], v[2:5]
	s_setprio 0
	s_barrier
	ds_read_b128 v[130:133], v175
	ds_read_b128 v[134:137], v175 offset:1024
	ds_read_b128 v[138:141], v175 offset:2048
	ds_read_b128 v[142:145], v175 offset:3072
	ds_read_b128 v[146:149], v176
	ds_read_b128 v[150:153], v176 offset:1024
	ds_read_b128 v[154:157], v176 offset:2048
	ds_read_b128 v[158:161], v176 offset:3072
	s_mov_b32 m0, s42
	ds_read_b128 v[178:181], v174 offset:32768
	ds_read_b128 v[182:185], v174 offset:33792
	ds_read_b128 v[186:189], v174 offset:34816
	ds_read_b128 v[190:193], v174 offset:35840
	ds_read_b128 v[194:197], v174 offset:36864
	ds_read_b128 v[198:201], v174 offset:37888
	ds_read_b128 v[202:205], v174 offset:38912
	ds_read_b128 v[206:209], v174 offset:39936
	buffer_load_dwordx4 v170, s[4:7], s82 offen lds
	s_mov_b32 m0, s43
	s_nop 0
	buffer_load_dwordx4 v171, s[4:7], s82 offen lds
	s_waitcnt vmcnt(8)
	s_waitcnt lgkmcnt(0)
	s_barrier
	s_setprio 1
	s_waitcnt lgkmcnt(7)
	v_mfma_f32_16x16x32_bf16 v[126:129], v[130:133], v[178:181], v[126:129]
	s_waitcnt lgkmcnt(6)
	v_mfma_f32_16x16x32_bf16 v[126:129], v[134:137], v[182:185], v[126:129]
	v_mfma_f32_16x16x32_bf16 v[122:125], v[138:141], v[178:181], v[122:125]
	s_nop 0
	v_mfma_f32_16x16x32_bf16 v[122:125], v[142:145], v[182:185], v[122:125]
	s_waitcnt lgkmcnt(5)
	v_mfma_f32_16x16x32_bf16 v[110:113], v[130:133], v[186:189], v[110:113]
	s_waitcnt lgkmcnt(4)
	v_mfma_f32_16x16x32_bf16 v[110:113], v[134:137], v[190:193], v[110:113]
	v_mfma_f32_16x16x32_bf16 v[106:109], v[138:141], v[186:189], v[106:109]
	s_nop 0
	v_mfma_f32_16x16x32_bf16 v[106:109], v[142:145], v[190:193], v[106:109]
	s_waitcnt lgkmcnt(3)
	v_mfma_f32_16x16x32_bf16 v[94:97], v[130:133], v[194:197], v[94:97]
	s_waitcnt lgkmcnt(2)
	v_mfma_f32_16x16x32_bf16 v[94:97], v[134:137], v[198:201], v[94:97]
	v_mfma_f32_16x16x32_bf16 v[90:93], v[138:141], v[194:197], v[90:93]
	s_nop 0
	v_mfma_f32_16x16x32_bf16 v[90:93], v[142:145], v[198:201], v[90:93]
	s_waitcnt lgkmcnt(1)
	v_mfma_f32_16x16x32_bf16 v[78:81], v[130:133], v[202:205], v[78:81]
	s_waitcnt lgkmcnt(0)
	v_mfma_f32_16x16x32_bf16 v[78:81], v[134:137], v[206:209], v[78:81]
	v_mfma_f32_16x16x32_bf16 v[74:77], v[138:141], v[202:205], v[74:77]
	s_nop 0
	v_mfma_f32_16x16x32_bf16 v[74:77], v[142:145], v[206:209], v[74:77]
	s_setprio 0
	s_setprio 1
	v_mfma_f32_16x16x32_bf16 v[118:121], v[146:149], v[178:181], v[118:121]
	s_nop 0
	v_mfma_f32_16x16x32_bf16 v[118:121], v[150:153], v[182:185], v[118:121]
	v_mfma_f32_16x16x32_bf16 v[114:117], v[154:157], v[178:181], v[114:117]
	s_nop 0
	v_mfma_f32_16x16x32_bf16 v[114:117], v[158:161], v[182:185], v[114:117]
	v_mfma_f32_16x16x32_bf16 v[102:105], v[146:149], v[186:189], v[102:105]
	s_nop 0
	v_mfma_f32_16x16x32_bf16 v[102:105], v[150:153], v[190:193], v[102:105]
	v_mfma_f32_16x16x32_bf16 v[98:101], v[154:157], v[186:189], v[98:101]
	s_nop 0
	v_mfma_f32_16x16x32_bf16 v[98:101], v[158:161], v[190:193], v[98:101]
	v_mfma_f32_16x16x32_bf16 v[86:89], v[146:149], v[194:197], v[86:89]
	s_nop 0
	v_mfma_f32_16x16x32_bf16 v[86:89], v[150:153], v[198:201], v[86:89]
	v_mfma_f32_16x16x32_bf16 v[82:85], v[154:157], v[194:197], v[82:85]
	s_nop 0
	v_mfma_f32_16x16x32_bf16 v[82:85], v[158:161], v[198:201], v[82:85]
	v_mfma_f32_16x16x32_bf16 v[70:73], v[146:149], v[202:205], v[70:73]
	s_nop 0
	v_mfma_f32_16x16x32_bf16 v[70:73], v[150:153], v[206:209], v[70:73]
	v_mfma_f32_16x16x32_bf16 v[66:69], v[154:157], v[202:205], v[66:69]
	s_nop 0
	v_mfma_f32_16x16x32_bf16 v[66:69], v[158:161], v[206:209], v[66:69]
	s_setprio 0
	s_barrier
; #define PG8_STAGE_A(bufoff, soff, voff) do { _Pragma("unroll") for (int _i = 0; _i < 2; ++_i) \
;         __builtin_amdgcn_raw_ptr_buffer_load_lds(rsA, (LAS void*)(lds + (bufoff) + ldsw + _i * 8192), 16, (voff)[_i], (soff), 0, 0); } while (0)
; #define PG8_STAGE_B(bufoff, soff) do { _Pragma("unroll") for (int _i = 0; _i < 2; ++_i) \
;         __builtin_amdgcn_raw_ptr_buffer_load_lds(rsB, (LAS void*)(lds + (bufoff) + ldsw + _i * 8192), 16, voffB[_i], (soff), 0, 0); } while (0)
; #define PG8_LDA(dst, b, h) do { _Pragma("unroll") for (int m = 0; m < 4; ++m) dst[m] = PG8_LD8(lds + PG8_SA(b, h) + aoff + m * 2048); } while (0)
; #define PG8_WAIT_V(n) asm volatile("s_waitcnt vmcnt(" #n ")" ::: "memory")
; #define PG8_WAIT_L(n) asm volatile("s_waitcnt lgkmcnt(" #n ")" ::: "memory")
; #define PG8_BAR __builtin_amdgcn_s_barrier()
; #define PG8_SCHED __builtin_amdgcn_sched_barrier(0)
; template <class Epi, class Sched, bool GATHER, bool ALIGN_EPI, bool SP2, bool FP8>
; __device__ __forceinline__ void gemm_phase(LAS unsigned char* lds, const Gemm g, const Sched& S, const Epi& E) {
;     ...
;         for (int t = 0; t < nt; t += 2) {
;             const bool last = (t == nt - 2);
;             if (last) pre = E.prefetch(cur, wr, wc, fr, fq);
;             const int a1 = cA + (t + 1) * kstep;
;             const int a2 = last ? nA : cA + (t + 2) * kstep, b2 = last ? nB : cB + (t + 2) * kstep;
;             const int a3 = a2 + kstep, b3 = b2 + kstep;
;     ...
;             PG8_LDA(At, 1, 1); PG8_STAGE_B(PG8_SB(1, 0), b3); PG8_STAGE_B(PG8_SB(1, 1), b3 + hstep); PG8_STAGE_A(PG8_SA(1, 0), a3, va20);
;             PG8_WAIT_V(8); PG8_WAIT_L(0); PG8_BAR; PG8_MMA(1, 0, At, B0); PG8_MMA(1, 1, At, B1); PG8_BAR; PG8_SCHED;
	s_mov_b32 m0, s46
	s_or_b32 s82, s81, 0x80
	ds_read_b128 v[178:181], v174 offset:49152
	ds_read_b128 v[182:185], v174 offset:50176
	ds_read_b128 v[186:189], v174 offset:51200
	ds_read_b128 v[190:193], v174 offset:52224
	ds_read_b128 v[194:197], v174 offset:53248
	ds_read_b128 v[198:201], v174 offset:54272
	ds_read_b128 v[202:205], v174 offset:55296
	ds_read_b128 v[206:209], v174 offset:56320
	buffer_load_dwordx4 v1, s[8:11], s82 offen lds
	s_mov_b32 m0, s47
	s_add_i32 s81, s81, 0x80080
	buffer_load_dwordx4 v163, s[8:11], s82 offen lds
	s_mov_b32 m0, s50
	s_nop 0
	buffer_load_dwordx4 v1, s[8:11], s81 offen lds
	s_mov_b32 m0, s51
	s_nop 0
	buffer_load_dwordx4 v163, s[8:11], s81 offen lds
	s_mov_b32 m0, s48
	s_nop 0
	buffer_load_dwordx4 v168, s[4:7], s80 offen lds
	s_mov_b32 m0, s49
	s_nop 0
	buffer_load_dwordx4 v169, s[4:7], s80 offen lds
	s_waitcnt vmcnt(8)
	s_waitcnt lgkmcnt(0)
	s_barrier
	s_setprio 1
	s_waitcnt lgkmcnt(7)
	v_mfma_f32_16x16x32_bf16 v[62:65], v[130:133], v[178:181], v[62:65]
	s_waitcnt lgkmcnt(6)
	v_mfma_f32_16x16x32_bf16 v[62:65], v[134:137], v[182:185], v[62:65]
	v_mfma_f32_16x16x32_bf16 v[58:61], v[138:141], v[178:181], v[58:61]
	s_nop 0
	v_mfma_f32_16x16x32_bf16 v[58:61], v[142:145], v[182:185], v[58:61]
	s_waitcnt lgkmcnt(5)
	v_mfma_f32_16x16x32_bf16 v[46:49], v[130:133], v[186:189], v[46:49]
	s_waitcnt lgkmcnt(4)
	v_mfma_f32_16x16x32_bf16 v[46:49], v[134:137], v[190:193], v[46:49]
	v_mfma_f32_16x16x32_bf16 v[42:45], v[138:141], v[186:189], v[42:45]
	s_nop 0
	v_mfma_f32_16x16x32_bf16 v[42:45], v[142:145], v[190:193], v[42:45]
	s_waitcnt lgkmcnt(3)
	v_mfma_f32_16x16x32_bf16 v[30:33], v[130:133], v[194:197], v[30:33]
	s_waitcnt lgkmcnt(2)
	v_mfma_f32_16x16x32_bf16 v[30:33], v[134:137], v[198:201], v[30:33]
	v_mfma_f32_16x16x32_bf16 v[26:29], v[138:141], v[194:197], v[26:29]
	s_nop 0
	v_mfma_f32_16x16x32_bf16 v[26:29], v[142:145], v[198:201], v[26:29]
	s_waitcnt lgkmcnt(1)
	v_mfma_f32_16x16x32_bf16 v[14:17], v[130:133], v[202:205], v[14:17]
	s_waitcnt lgkmcnt(0)
	v_mfma_f32_16x16x32_bf16 v[14:17], v[134:137], v[206:209], v[14:17]
	v_mfma_f32_16x16x32_bf16 v[10:13], v[138:141], v[202:205], v[10:13]
	s_nop 0
	v_mfma_f32_16x16x32_bf16 v[10:13], v[142:145], v[206:209], v[10:13]
	s_setprio 0
	s_setprio 1
	v_mfma_f32_16x16x32_bf16 v[54:57], v[146:149], v[178:181], v[54:57]
	s_nop 0
	v_mfma_f32_16x16x32_bf16 v[54:57], v[150:153], v[182:185], v[54:57]
	v_mfma_f32_16x16x32_bf16 v[50:53], v[154:157], v[178:181], v[50:53]
	s_nop 0
	v_mfma_f32_16x16x32_bf16 v[50:53], v[158:161], v[182:185], v[50:53]
	v_mfma_f32_16x16x32_bf16 v[38:41], v[146:149], v[186:189], v[38:41]
	s_nop 0
	v_mfma_f32_16x16x32_bf16 v[38:41], v[150:153], v[190:193], v[38:41]
	v_mfma_f32_16x16x32_bf16 v[34:37], v[154:157], v[186:189], v[34:37]
	s_nop 0
	v_mfma_f32_16x16x32_bf16 v[34:37], v[158:161], v[190:193], v[34:37]
	v_mfma_f32_16x16x32_bf16 v[22:25], v[146:149], v[194:197], v[22:25]
	s_nop 0
	v_mfma_f32_16x16x32_bf16 v[22:25], v[150:153], v[198:201], v[22:25]
	v_mfma_f32_16x16x32_bf16 v[18:21], v[154:157], v[194:197], v[18:21]
	s_nop 0
	v_mfma_f32_16x16x32_bf16 v[18:21], v[158:161], v[198:201], v[18:21]
	v_mfma_f32_16x16x32_bf16 v[6:9], v[146:149], v[202:205], v[6:9]
	s_nop 0
	v_mfma_f32_16x16x32_bf16 v[6:9], v[150:153], v[206:209], v[6:9]
	v_mfma_f32_16x16x32_bf16 v[2:5], v[154:157], v[202:205], v[2:5]
	s_nop 0
	v_mfma_f32_16x16x32_bf16 v[2:5], v[158:161], v[206:209], v[2:5]
	s_setprio 0
	s_barrier
	s_add_i32 s79, s79, 2
	s_addk_i32 s77, 0x100
	s_addk_i32 s78, 0x100
	s_cmp_gt_u32 s79, 29
